# fp8 A fragments stored as [kstep][half][lane][16B] so every A load instruction is one fully coalesced 1 KiB
# speedup vs baseline: 1.0069x; 1.0069x over previous
.LBB0_34:
	s_andn2_b64 vcc, exec, s[8:9]
	s_cbranch_vccnz .LBB0_38
	v_lshrrev_b32_e32 v1, 2, v0
	s_ashr_i32 s3, s3, 3
	s_lshl_b32 s8, s2, 5
	s_and_b32 s8, s8, 0xe0
	v_lshrrev_b32_e32 v2, 3, v0
	v_and_b32_e32 v3, 7, v0
	v_lshlrev_b32_e32 v4, 13, v2
	v_lshl_or_b32 v4, v3, 4, v4
	v_add_u32_e32 v5, 0x1000, v4
	s_waitcnt lgkmcnt(0)
	s_lshl_b32 s9, s3, 7
	s_add_u32 s10, s6, s9
	s_addc_u32 s11, s7, 0
	s_lshl_b32 s9, s8, 2
	s_add_u32 s12, s4, s9
	s_addc_u32 s13, s5, 0
	global_load_dwordx4 v[16:19], v4, s[10:11]
	global_load_dwordx4 v[20:23], v4, s[10:11] offset:1024
	global_load_dwordx4 v[24:27], v4, s[10:11] offset:2048
	global_load_dwordx4 v[28:31], v4, s[10:11] offset:3072
	global_load_dwordx4 v[32:35], v5, s[10:11]
	global_load_dwordx4 v[36:39], v5, s[10:11] offset:1024
	global_load_dwordx4 v[40:43], v5, s[10:11] offset:2048
	global_load_dwordx4 v[44:47], v5, s[10:11] offset:3072
	global_load_dwordx4 v[48:51], v4, s[12:13]
	global_load_dwordx4 v[52:55], v4, s[12:13] offset:1024
	global_load_dwordx4 v[56:59], v4, s[12:13] offset:2048
	global_load_dwordx4 v[60:63], v4, s[12:13] offset:3072
	global_load_dwordx4 v[64:67], v5, s[12:13]
	global_load_dwordx4 v[68:71], v5, s[12:13] offset:1024
	global_load_dwordx4 v[72:75], v5, s[12:13] offset:2048
	global_load_dwordx4 v[76:79], v5, s[12:13] offset:3072
	v_mul_u32_u24_e32 v6, 0x840, v3
	v_lshl_add_u32 v6, v2, 4, v6
	v_add_u32_e32 v6, 0x4000, v6
	v_and_b32_e32 v8, 31, v0
	v_lshrrev_b32_e32 v9, 6, v0
	v_bfe_u32 v10, v0, 5, 1
	v_lshl_or_b32 v9, v9, 3, v10
	v_mul_u32_u24_e32 v7, 0x210, v8
	v_lshl_add_u32 v7, v9, 4, v7
	v_add_u32_e32 v7, 0x4000, v7
	s_waitcnt vmcnt(8)
	v_cvt_pk_f16_f32 v80, v16, v20
	v_cvt_pk_f16_f32 v81, v24, v28
	v_cvt_pk_f16_f32 v82, v32, v36
	v_cvt_pk_f16_f32 v83, v40, v44
	ds_write_b128 v6, v[80:83]
	v_cvt_pk_f16_f32 v84, v17, v21
	v_cvt_pk_f16_f32 v85, v25, v29
	v_cvt_pk_f16_f32 v86, v33, v37
	v_cvt_pk_f16_f32 v87, v41, v45
	ds_write_b128 v6, v[84:87] offset:528
	v_cvt_pk_f16_f32 v88, v18, v22
	v_cvt_pk_f16_f32 v89, v26, v30
	v_cvt_pk_f16_f32 v90, v34, v38
	v_cvt_pk_f16_f32 v91, v42, v46
	ds_write_b128 v6, v[88:91] offset:1056
	v_cvt_pk_f16_f32 v92, v19, v23
	v_cvt_pk_f16_f32 v93, v27, v31
	v_cvt_pk_f16_f32 v94, v35, v39
	v_cvt_pk_f16_f32 v95, v43, v47
	ds_write_b128 v6, v[92:95] offset:1584
	s_waitcnt vmcnt(0)
	v_cvt_pk_f16_f32 v80, v48, v52
	v_cvt_pk_f16_f32 v81, v56, v60
	v_cvt_pk_f16_f32 v82, v64, v68
	v_cvt_pk_f16_f32 v83, v72, v76
	ds_write_b128 v6, v[80:83] offset:16896
	v_cvt_pk_f16_f32 v84, v49, v53
	v_cvt_pk_f16_f32 v85, v57, v61
	v_cvt_pk_f16_f32 v86, v65, v69
	v_cvt_pk_f16_f32 v87, v73, v77
	ds_write_b128 v6, v[84:87] offset:17424
	v_cvt_pk_f16_f32 v88, v50, v54
	v_cvt_pk_f16_f32 v89, v58, v62
	v_cvt_pk_f16_f32 v90, v66, v70
	v_cvt_pk_f16_f32 v91, v74, v78
	ds_write_b128 v6, v[88:91] offset:17952
	v_cvt_pk_f16_f32 v92, v51, v55
	v_cvt_pk_f16_f32 v93, v59, v63
	v_cvt_pk_f16_f32 v94, v67, v71
	v_cvt_pk_f16_f32 v95, v75, v79
	ds_write_b128 v6, v[92:95] offset:18480
	s_waitcnt lgkmcnt(0)
	s_barrier
	ds_read_b128 v[16:19], v7
	ds_read_b128 v[32:35], v7 offset:16896
	ds_read_b128 v[20:23], v7 offset:32
	ds_read_b128 v[36:39], v7 offset:16928
	ds_read_b128 v[24:27], v7 offset:64
	ds_read_b128 v[40:43], v7 offset:16960
	ds_read_b128 v[28:31], v7 offset:96
	ds_read_b128 v[44:47], v7 offset:16992
	s_waitcnt lgkmcnt(6)
	v_mfma_f32_32x32x16_f16 a[0:15], v[16:19], v[32:35], 0
	s_waitcnt lgkmcnt(4)
	v_mfma_f32_32x32x16_f16 a[0:15], v[20:23], v[36:39], a[0:15]
	s_waitcnt lgkmcnt(2)
	v_mfma_f32_32x32x16_f16 a[0:15], v[24:27], v[40:43], a[0:15]
	s_waitcnt lgkmcnt(0)
	v_mfma_f32_32x32x16_f16 a[0:15], v[28:31], v[44:47], a[0:15]
	v_lshrrev_b32_e32 v2, 6, v0
	v_and_b32_e32 v3, 63, v0
	v_lshlrev_b32_e32 v2, 12, v2
	v_lshl_or_b32 v2, v3, 2, v2
	s_movk_i32 s4, 0x80
	v_cmp_gt_u32_e32 vcc, s4, v0
	s_nop 7
	ds_write_b32 v2, a0
	ds_write_b32 v2, a1 offset:256
	ds_write_b32 v2, a2 offset:512
	ds_write_b32 v2, a3 offset:768
	ds_write_b32 v2, a4 offset:1024
	ds_write_b32 v2, a5 offset:1280
	ds_write_b32 v2, a6 offset:1536
	ds_write_b32 v2, a7 offset:1792
	ds_write_b32 v2, a8 offset:2048
	ds_write_b32 v2, a9 offset:2304
	ds_write_b32 v2, a10 offset:2560
	ds_write_b32 v2, a11 offset:2816
	ds_write_b32 v2, a12 offset:3072
	ds_write_b32 v2, a13 offset:3328
	ds_write_b32 v2, a14 offset:3584
	ds_write_b32 v2, a15 offset:3840
	s_waitcnt lgkmcnt(0)
	s_barrier
	s_and_saveexec_b64 s[4:5], vcc
	s_cbranch_execz .LBB0_37
	v_lshrrev_b32_e32 v2, 3, v0
	v_and_b32_e32 v2, 12, v2
	v_and_b32_e32 v34, 3, v0
	v_and_or_b32 v2, v1, 3, v2
	v_lshlrev_b32_e32 v3, 3, v0
	v_and_b32_e32 v3, 0x80, v3
	v_lshlrev_b32_e32 v4, 5, v34
	v_lshlrev_b32_e32 v2, 8, v2
	v_or3_b32 v30, v3, v4, v2
	ds_read_b128 v[2:5], v30 offset:4096
	ds_read_b128 v[6:9], v30
	ds_read_b128 v[10:13], v30 offset:16
	ds_read_b128 v[14:17], v30 offset:8192
	ds_read_b128 v[18:21], v30 offset:12288
	ds_read_b128 v[22:25], v30 offset:4112
	s_waitcnt lgkmcnt(4)
	v_add_f32_e32 v2, v6, v2
	ds_read_b128 v[26:29], v30 offset:8208
	s_waitcnt lgkmcnt(3)
	v_add_f32_e32 v2, v2, v14
	s_waitcnt lgkmcnt(2)
	v_add_f32_e32 v2, v2, v18
	v_mul_f32_e32 v6, 0x43000000, v2
	v_add_f32_e32 v2, v7, v3
	v_add_f32_e32 v2, v2, v15
	v_add_f32_e32 v2, v2, v19
	v_mul_f32_e32 v7, 0x43000000, v2
	v_add_f32_e32 v2, v8, v4
	v_add_f32_e32 v2, v2, v16
	v_add_f32_e32 v2, v2, v20
	ds_read_b128 v[30:33], v30 offset:12304
	v_mul_f32_e32 v4, 0x43000000, v2
	v_add_f32_e32 v2, v9, v5
	v_add_f32_e32 v2, v2, v17
	v_add_f32_e32 v2, v2, v21
	v_mul_f32_e32 v5, 0x43000000, v2
	s_waitcnt lgkmcnt(2)
	v_add_f32_e32 v2, v10, v22
	s_waitcnt lgkmcnt(1)
	v_add_f32_e32 v2, v2, v26
	s_waitcnt lgkmcnt(0)
	v_add_f32_e32 v2, v2, v30
	v_mul_f32_e32 v8, 0x43000000, v2
	v_add_f32_e32 v2, v11, v23
	v_add_f32_e32 v2, v2, v27
	v_add_f32_e32 v2, v2, v31
	v_mul_f32_e32 v9, 0x43000000, v2
	v_add_f32_e32 v2, v12, v24
	v_add_f32_e32 v2, v2, v28
	v_add_f32_e32 v2, v2, v32
	v_mul_f32_e32 v10, 0x43000000, v2
	v_add_f32_e32 v2, v13, v25
	v_add_f32_e32 v11, v2, v29
	v_mov_b32_e32 v3, 0
	v_mov_b32_e32 v2, 0
	v_cvt_pk_fp8_f32 v2, v6, v7
	v_cvt_pk_fp8_f32 v3, v8, v9
	v_add_f32_e32 v6, v11, v33
	s_load_dwordx2 s[6:7], s[0:1], 0x38
	v_mul_f32_e32 v6, 0x43000000, v6
	v_cvt_pk_fp8_f32 v2, v4, v5 op_sel:[0,0,1]
	v_cvt_pk_fp8_f32 v3, v10, v6 op_sel:[0,0,1]
	s_lshl_b32 s12, s3, 13
	s_lshr_b32 s13, s8, 6
	s_lshl_b32 s13, s13, 11
	s_or_b32 s12, s12, s13
	s_and_b32 s13, s8, 32
	s_lshl_b32 s13, s13, 4
	s_or_b32 s12, s12, s13
	v_lshrrev_b32_e32 v35, 1, v34
	v_lshlrev_b32_e32 v35, 10, v35
	v_lshl_or_b32 v35, v1, 4, v35
	v_and_b32_e32 v36, 1, v34
	v_lshl_or_b32 v35, v36, 3, v35
	v_or_b32_e32 v35, s12, v35
	v_and_b32_e32 v35, 0xfff8, v35
	s_lshl_b32 s3, s3, 8
	s_or_b32 s3, s3, s8
	v_lshlrev_b32_e32 v4, 3, v34
	v_or_b32_e32 v1, s3, v1
	v_lshl_or_b32 v1, v1, 5, v4
	s_waitcnt lgkmcnt(0)
	global_store_dwordx2 v35, v[2:3], s[6:7]

_Z7na_mainPKDF16_PKhS0_PKfS4_S4_S4_Pf:
	s_lshl_b32 s3, s2, 5
	s_and_b32 s3, s3, 0xe0
	s_ashr_i32 s2, s2, 3
	s_add_i32 s3, s3, s2
	s_ashr_i32 s2, s3, 6
	s_lshl_b32 s3, s3, 5
	s_and_b32 s14, s3, 0x7e0
	v_mov_b32_e32 v1, 0x7c0
	s_load_dwordx8 s[4:11], s[0:1], 0x0
	s_load_dwordx2 s[18:19], s[0:1], 0x20
	s_load_dwordx2 s[28:29], s[0:1], 0x28
	s_load_dwordx2 s[34:35], s[0:1], 0x30
	s_load_dwordx2 s[30:31], s[0:1], 0x38
	v_med3_u32 v1, s14, 32, v1
	v_subrev_u32_e32 v97, 32, v1
	s_ashr_i32 s3, s2, 31
	v_lshlrev_b32_e32 v58, 1, v97
	s_lshl_b64 s[12:13], s[2:3], 12
	v_mov_b32_e32 v59, 0
	v_sub_u32_e32 v60, s14, v97
	v_lshl_add_u64 v[10:11], s[12:13], 0, v[58:59]
	v_lshlrev_b64 v[2:3], 9, v[10:11]
	v_lshl_or_b32 v22, v60, 6, v0
	s_waitcnt lgkmcnt(0)
	s_load_dword s32, s[28:29], 0x0
	v_and_b32_e32 v208, 31, v0
	v_lshlrev_b32_e32 v208, 5, v208
	global_load_dwordx4 v[192:195], v208, s[18:19]
	global_load_dwordx4 v[196:199], v208, s[18:19] offset:16
	v_lshl_add_u64 v[20:21], s[4:5], 0, v[2:3]
	v_ashrrev_i32_e32 v23, 31, v22
	v_lshl_add_u64 v[2:3], v[22:23], 4, v[20:21]
	global_load_dwordx4 v[12:15], v[2:3], off
	v_or_b32_e32 v28, 0x200, v22
	v_ashrrev_i32_e32 v29, 31, v28
	v_lshl_add_u64 v[2:3], v[28:29], 4, v[20:21]
	global_load_dwordx4 v[16:19], v[2:3], off
	v_or_b32_e32 v184, 0x400, v22
	v_ashrrev_i32_e32 v185, 31, v184
	v_lshl_add_u64 v[184:185], v[184:185], 4, v[20:21]
	v_or_b32_e32 v188, 0x600, v22
	v_ashrrev_i32_e32 v189, 31, v188
	v_lshl_add_u64 v[188:189], v[188:189], 4, v[20:21]
	global_load_dwordx4 v[184:187], v[184:185], off
	global_load_dwordx4 v[188:191], v[188:189], off
	v_lshrrev_b32_e32 v99, 6, v0
	v_and_b32_e32 v98, 63, v0
	v_lshlrev_b32_e32 v118, 13, v99
	v_lshl_or_b32 v58, v98, 4, v118
	v_and_b32_e32 v58, 0xfff0, v58
	v_add_u32_e32 v251, 0x1000, v58
	s_movk_i32 s15, 0x1000
	v_lshl_add_u64 v[24:25], s[6:7], 0, v[58:59]
	v_or_b32_e32 v32, 0x400, v22
	v_or_b32_e32 v62, 0x600, v22
	v_add_co_u32_e32 v64, vcc, s15, v24
	s_mov_b64 s[12:13], 0x1000
	s_mov_b64 s[16:17], 0x1800
	v_lshlrev_b32_e32 v72, 1, v60
	v_lshrrev_b32_e32 v23, 5, v22
	v_and_b32_e32 v34, 32, v22
	v_ashrrev_i32_e32 v33, 31, v32
	v_ashrrev_i32_e32 v63, 31, v62
	v_addc_co_u32_e32 v65, vcc, 0, v25, vcc
	global_load_dwordx4 v[6:9], v58, s[6:7] offset:1024
	global_load_dwordx4 v[2:5], v58, s[6:7]
	global_load_dwordx4 v[54:57], v58, s[6:7] offset:3072
	global_load_dwordx4 v[50:53], v58, s[6:7] offset:2048
	v_lshrrev_b32_e32 v58, 6, v22
	v_bfe_u32 v73, v22, 8, 2
	v_lshl_add_u64 v[26:27], v[24:25], 0, s[12:13]
	v_lshl_add_u64 v[24:25], v[24:25], 0, s[16:17]
	v_cmp_ne_u32_e32 vcc, 0, v34
	v_sub_u32_e32 v75, v23, v72
	global_load_dwordx4 v[42:45], v251, s[6:7]
	global_load_dwordx4 v[46:49], v251, s[6:7] offset:1024
	global_load_dwordx4 v[34:37], v251, s[6:7] offset:2048
	global_load_dwordx4 v[38:41], v251, s[6:7] offset:3072
	v_mov_b32_e32 v61, 0x60
	v_cndmask_b32_e32 v74, 0, v61, vcc
	v_add_u32_e32 v33, v74, v58
	v_lshlrev_b32_e32 v64, 2, v33
	v_bfe_u32 v96, v0, 4, 1
	v_and_b32_e32 v100, 15, v0
	v_mov_b32_e32 v30, v59
	v_mov_b32_e32 v31, v59
	v_and_b32_e32 v64, 12, v64
	v_mul_u32_u24_e32 v29, 0xc000, v96
	v_bitop3_b32 v64, v64, v100, v73 bitop3:0x36
	v_lshl_or_b32 v64, v64, 4, v29
	v_lshlrev_b32_e32 v63, 1, v75
	v_lshl_add_u32 v33, v33, 8, v64
	v_bfe_u32 v71, v0, 1, 4
	v_and_b32_e32 v70, 32, v0
	v_lshlrev_b32_e32 v1, 3, v0
	v_lshrrev_b32_e32 v58, 1, v75
	v_and_b32_e32 v1, 8, v1
	v_add_lshl_u32 v58, v58, v70, 8
	v_lshlrev_b32_e32 v121, 3, v99
	v_bfe_u32 v101, v0, 4, 2
	v_lshlrev_b32_e32 v102, 2, v101
	v_and_b32_e32 v116, 31, v0
	v_bfe_u32 v119, v0, 5, 1
	v_lshlrev_b32_e32 v124, 1, v119
	v_lshlrev_b32_e32 v117, 8, v116
	v_lshrrev_b32_e32 v95, 4, v0
	s_movk_i32 s16, 0x60
	s_mov_b32 s17, 0xc000
	v_and_b32_e32 v211, 3, v99
	v_lshrrev_b32_e32 v212, 2, v99
	v_lshl_or_b32 v211, v211, 2, v212
	v_xor_b32_e32 v213, v100, v211
	v_mul_u32_u24_e32 v214, 0x60, v119
	v_add3_u32 v214, v214, v60, v99
	v_mul_u32_u24_e32 v215, 0xc000, v96
	v_lshl_add_u32 v214, v214, 8, v215
	v_lshl_or_b32 v220, v213, 4, v214
	v_xor_b32_e32 v221, 32, v220
	v_xor_b32_e32 v216, v71, v211
	v_lshl_add_u32 v217, v119, 5, v99
	v_lshlrev_b32_e32 v217, 8, v217
	v_lshl_or_b32 v216, v216, 4, v217
	v_or_b32_e32 v216, v216, v1
	v_add_u32_e32 v222, 0x23800, v216
	v_xor_b32_e32 v223, 32, v222
	s_waitcnt vmcnt(11)
	ds_write_b128 v220, v[12:15]
	v_fma_mix_f32 v200, v192, v12, 0 op_sel_hi:[0,1,0]
	v_fma_mix_f32 v201, v193, v12, 0 op_sel:[0,1,0] op_sel_hi:[0,1,0]
	v_cvt_f32_f16_e32 v211, v12
	v_cvt_f32_f16_sdwa v212, v12 dst_sel:DWORD dst_unused:UNUSED_PAD src0_sel:WORD_1
	v_fma_mix_f32 v200, v194, v13, v200 op_sel_hi:[0,1,0]
	v_fma_mix_f32 v201, v195, v13, v201 op_sel:[0,1,0] op_sel_hi:[0,1,0]
	v_cvt_f32_f16_e32 v213, v13
	v_cvt_f32_f16_sdwa v214, v13 dst_sel:DWORD dst_unused:UNUSED_PAD src0_sel:WORD_1
	v_fma_mix_f32 v200, v196, v14, v200 op_sel_hi:[0,1,0]
	v_fma_mix_f32 v201, v197, v14, v201 op_sel:[0,1,0] op_sel_hi:[0,1,0]
	v_cvt_f32_f16_e32 v215, v14
	v_cvt_f32_f16_sdwa v216, v14 dst_sel:DWORD dst_unused:UNUSED_PAD src0_sel:WORD_1
	v_fma_mix_f32 v200, v198, v15, v200 op_sel_hi:[0,1,0]
	v_fma_mix_f32 v201, v199, v15, v201 op_sel:[0,1,0] op_sel_hi:[0,1,0]
	v_cvt_f32_f16_e32 v217, v15
	v_cvt_f32_f16_sdwa v218, v15 dst_sel:DWORD dst_unused:UNUSED_PAD src0_sel:WORD_1
	v_cvt_pk_fp8_f32 v224, v211, v212
	v_cvt_pk_fp8_f32 v225, v215, v216
	v_cvt_pk_fp8_f32 v224, v213, v214 op_sel:[0,0,1]
	v_cvt_pk_fp8_f32 v225, v217, v218 op_sel:[0,0,1]
	s_nop 0
	ds_write_b64 v222, v[224:225]
	s_waitcnt vmcnt(10)
	ds_write_b128 v221, v[16:19] offset:2048
	v_fma_mix_f32 v202, v192, v16, 0 op_sel_hi:[0,1,0]
	v_fma_mix_f32 v203, v193, v16, 0 op_sel:[0,1,0] op_sel_hi:[0,1,0]
	v_cvt_f32_f16_e32 v211, v16
	v_cvt_f32_f16_sdwa v212, v16 dst_sel:DWORD dst_unused:UNUSED_PAD src0_sel:WORD_1
	v_fma_mix_f32 v202, v194, v17, v202 op_sel_hi:[0,1,0]
	v_fma_mix_f32 v203, v195, v17, v203 op_sel:[0,1,0] op_sel_hi:[0,1,0]
	v_cvt_f32_f16_e32 v213, v17
	v_cvt_f32_f16_sdwa v214, v17 dst_sel:DWORD dst_unused:UNUSED_PAD src0_sel:WORD_1
	v_fma_mix_f32 v202, v196, v18, v202 op_sel_hi:[0,1,0]
	v_fma_mix_f32 v203, v197, v18, v203 op_sel:[0,1,0] op_sel_hi:[0,1,0]
	v_cvt_f32_f16_e32 v215, v18
	v_cvt_f32_f16_sdwa v216, v18 dst_sel:DWORD dst_unused:UNUSED_PAD src0_sel:WORD_1
	v_fma_mix_f32 v202, v198, v19, v202 op_sel_hi:[0,1,0]
	v_fma_mix_f32 v203, v199, v19, v203 op_sel:[0,1,0] op_sel_hi:[0,1,0]
	v_cvt_f32_f16_e32 v217, v19
	v_cvt_f32_f16_sdwa v218, v19 dst_sel:DWORD dst_unused:UNUSED_PAD src0_sel:WORD_1
	v_cvt_pk_fp8_f32 v226, v211, v212
	v_cvt_pk_fp8_f32 v227, v215, v216
	v_cvt_pk_fp8_f32 v226, v213, v214 op_sel:[0,0,1]
	v_cvt_pk_fp8_f32 v227, v217, v218 op_sel:[0,0,1]
	s_nop 0
	ds_write_b64 v223, v[226:227] offset:2048
	s_waitcnt vmcnt(9)
	ds_write_b128 v220, v[184:187] offset:4096
	v_fma_mix_f32 v204, v192, v184, 0 op_sel_hi:[0,1,0]
	v_fma_mix_f32 v205, v193, v184, 0 op_sel:[0,1,0] op_sel_hi:[0,1,0]
	v_cvt_f32_f16_e32 v211, v184
	v_cvt_f32_f16_sdwa v212, v184 dst_sel:DWORD dst_unused:UNUSED_PAD src0_sel:WORD_1
	v_fma_mix_f32 v204, v194, v185, v204 op_sel_hi:[0,1,0]
	v_fma_mix_f32 v205, v195, v185, v205 op_sel:[0,1,0] op_sel_hi:[0,1,0]
	v_cvt_f32_f16_e32 v213, v185
	v_cvt_f32_f16_sdwa v214, v185 dst_sel:DWORD dst_unused:UNUSED_PAD src0_sel:WORD_1
	v_fma_mix_f32 v204, v196, v186, v204 op_sel_hi:[0,1,0]
	v_fma_mix_f32 v205, v197, v186, v205 op_sel:[0,1,0] op_sel_hi:[0,1,0]
	v_cvt_f32_f16_e32 v215, v186
	v_cvt_f32_f16_sdwa v216, v186 dst_sel:DWORD dst_unused:UNUSED_PAD src0_sel:WORD_1
	v_fma_mix_f32 v204, v198, v187, v204 op_sel_hi:[0,1,0]
	v_fma_mix_f32 v205, v199, v187, v205 op_sel:[0,1,0] op_sel_hi:[0,1,0]
	v_cvt_f32_f16_e32 v217, v187
	v_cvt_f32_f16_sdwa v218, v187 dst_sel:DWORD dst_unused:UNUSED_PAD src0_sel:WORD_1
	v_cvt_pk_fp8_f32 v228, v211, v212
	v_cvt_pk_fp8_f32 v229, v215, v216
	v_cvt_pk_fp8_f32 v228, v213, v214 op_sel:[0,0,1]
	v_cvt_pk_fp8_f32 v229, v217, v218 op_sel:[0,0,1]
	s_nop 0
	ds_write_b64 v222, v[228:229] offset:4096
	s_waitcnt vmcnt(8)
	ds_write_b128 v221, v[188:191] offset:6144
	v_fma_mix_f32 v206, v192, v188, 0 op_sel_hi:[0,1,0]
	v_fma_mix_f32 v207, v193, v188, 0 op_sel:[0,1,0] op_sel_hi:[0,1,0]
	v_cvt_f32_f16_e32 v211, v188
	v_cvt_f32_f16_sdwa v212, v188 dst_sel:DWORD dst_unused:UNUSED_PAD src0_sel:WORD_1
	v_fma_mix_f32 v206, v194, v189, v206 op_sel_hi:[0,1,0]
	v_fma_mix_f32 v207, v195, v189, v207 op_sel:[0,1,0] op_sel_hi:[0,1,0]
	v_cvt_f32_f16_e32 v213, v189
	v_cvt_f32_f16_sdwa v214, v189 dst_sel:DWORD dst_unused:UNUSED_PAD src0_sel:WORD_1
	v_fma_mix_f32 v206, v196, v190, v206 op_sel_hi:[0,1,0]
	v_fma_mix_f32 v207, v197, v190, v207 op_sel:[0,1,0] op_sel_hi:[0,1,0]
	v_cvt_f32_f16_e32 v215, v190
	v_cvt_f32_f16_sdwa v216, v190 dst_sel:DWORD dst_unused:UNUSED_PAD src0_sel:WORD_1
	v_fma_mix_f32 v206, v198, v191, v206 op_sel_hi:[0,1,0]
	v_fma_mix_f32 v207, v199, v191, v207 op_sel:[0,1,0] op_sel_hi:[0,1,0]
	v_cvt_f32_f16_e32 v217, v191
	v_cvt_f32_f16_sdwa v218, v191 dst_sel:DWORD dst_unused:UNUSED_PAD src0_sel:WORD_1
	v_cvt_pk_fp8_f32 v230, v211, v212
	v_cvt_pk_fp8_f32 v231, v215, v216
	v_cvt_pk_fp8_f32 v230, v213, v214 op_sel:[0,0,1]
	v_cvt_pk_fp8_f32 v231, v217, v218 op_sel:[0,0,1]
	s_nop 0
	ds_write_b64 v223, v[230:231] offset:6144
	v_add_f32_e32 v200, v200, v201
	v_add_f32_e32 v202, v202, v203
	v_add_f32_e32 v204, v204, v205
	v_add_f32_e32 v206, v206, v207
	v_lshlrev_b32_e32 v208, 7, v119
	v_lshl_add_u32 v208, v99, 2, v208
	v_add_u32_e32 v208, 0x27800, v208
	v_add_f32_dpp v200, v200, v200 quad_perm:[1,0,3,2] row_mask:0xf bank_mask:0xf
	v_add_f32_dpp v202, v202, v202 quad_perm:[1,0,3,2] row_mask:0xf bank_mask:0xf
	v_add_f32_dpp v204, v204, v204 quad_perm:[1,0,3,2] row_mask:0xf bank_mask:0xf
	v_add_f32_dpp v206, v206, v206 quad_perm:[1,0,3,2] row_mask:0xf bank_mask:0xf
	v_add_f32_dpp v200, v200, v200 quad_perm:[2,3,0,1] row_mask:0xf bank_mask:0xf
	v_add_f32_dpp v202, v202, v202 quad_perm:[2,3,0,1] row_mask:0xf bank_mask:0xf
	v_add_f32_dpp v204, v204, v204 quad_perm:[2,3,0,1] row_mask:0xf bank_mask:0xf
	v_add_f32_dpp v206, v206, v206 quad_perm:[2,3,0,1] row_mask:0xf bank_mask:0xf
	v_add_f32_dpp v200, v200, v200 row_half_mirror row_mask:0xf bank_mask:0xf
	v_add_f32_dpp v202, v202, v202 row_half_mirror row_mask:0xf bank_mask:0xf
	v_add_f32_dpp v204, v204, v204 row_half_mirror row_mask:0xf bank_mask:0xf
	v_add_f32_dpp v206, v206, v206 row_half_mirror row_mask:0xf bank_mask:0xf
	v_add_f32_dpp v200, v200, v200 row_mirror row_mask:0xf bank_mask:0xf
	v_add_f32_dpp v202, v202, v202 row_mirror row_mask:0xf bank_mask:0xf
	v_add_f32_dpp v204, v204, v204 row_mirror row_mask:0xf bank_mask:0xf
	v_add_f32_dpp v206, v206, v206 row_mirror row_mask:0xf bank_mask:0xf
	v_add_f32_dpp v200, v200, v200 row_bcast:15 row_mask:0xa bank_mask:0xf
	v_add_f32_dpp v202, v202, v202 row_bcast:15 row_mask:0xa bank_mask:0xf
	v_add_f32_dpp v204, v204, v204 row_bcast:15 row_mask:0xa bank_mask:0xf
	v_add_f32_dpp v206, v206, v206 row_bcast:15 row_mask:0xa bank_mask:0xf
	s_mov_b32 exec_lo, 0xffff0000
	s_mov_b32 exec_hi, 0xffff0000
	ds_write_b32 v208, v200
	ds_write_b32 v208, v202 offset:32
	ds_write_b32 v208, v204 offset:64
	ds_write_b32 v208, v206 offset:96
	s_mov_b64 exec, -1
	v_lshlrev_b32_e32 v201, 7, v99
	v_lshl_or_b32 v201, v119, 4, v201
	global_load_dwordx4 v[184:187], v201, s[10:11]
	global_load_dwordx4 v[188:191], v201, s[10:11] offset:32
	global_load_dwordx4 v[192:195], v201, s[10:11] offset:64
	global_load_dwordx4 v[196:199], v201, s[10:11] offset:96
	v_cmp_lt_i32_e32 vcc, v121, v60
	s_nop 0
	v_mov_b32_e32 v15, v59
	v_cndmask_b32_e64 v12, 32, 0, vcc
	v_add_u32_e32 v16, v12, v121
	v_or_b32_e32 v12, v16, v101
	v_lshlrev_b32_e32 v58, 1, v12
	v_lshrrev_b32_e32 v12, 5, v0
	v_and_b32_e32 v12, 2, v12
	v_bitop3_b32 v14, v102, v100, v12 bitop3:0x36
	v_lshl_add_u64 v[12:13], v[10:11], 0, v[58:59]
	v_lshlrev_b64 v[12:13], 9, v[12:13]
	v_lshlrev_b32_e32 v16, 8, v16
	v_lshl_add_u64 v[12:13], s[4:5], 0, v[12:13]
	v_lshlrev_b32_e32 v14, 4, v14
	v_readfirstlane_b32 s6, v16
	v_add_u32_e32 v17, 0xc000, v16
	v_lshl_add_u64 v[12:13], v[12:13], 0, v[14:15]
	s_mov_b32 m0, s6
	s_mov_b64 s[6:7], 0x100
	v_readfirstlane_b32 s12, v17
	global_load_lds_dwordx4 v[12:13], off
	v_lshl_add_u64 v[12:13], v[12:13], 0, s[6:7]
	s_mov_b32 m0, s12
	v_or_b32_e32 v58, 1, v58
	global_load_lds_dwordx4 v[12:13], off
	v_lshl_add_u64 v[12:13], v[10:11], 0, v[58:59]
	v_lshlrev_b64 v[12:13], 9, v[12:13]
	v_lshl_add_u64 v[12:13], s[4:5], 0, v[12:13]
	v_lshl_add_u64 v[12:13], v[12:13], 0, v[14:15]
	v_add_u32_e32 v14, 0x6000, v16
	v_bfe_u32 v61, v0, 2, 2
	v_readfirstlane_b32 s12, v14
	v_add_u32_e32 v14, 0x12000, v16
	s_mov_b32 m0, s12
	v_readfirstlane_b32 s12, v14
	global_load_lds_dwordx4 v[12:13], off
	v_lshl_add_u64 v[12:13], v[12:13], 0, s[6:7]
	s_mov_b32 m0, s12
	v_add_u32_e32 v18, 0x23800, v117
	global_load_lds_dwordx4 v[12:13], off
	v_or_b32_e32 v12, 4, v121
	v_cmp_lt_i32_e32 vcc, v12, v60
	s_nop 1
	v_cndmask_b32_e64 v13, 32, 0, vcc
	v_add_u32_e32 v16, v13, v12
	v_or_b32_e32 v13, v16, v101
	v_lshlrev_b32_e32 v58, 1, v13
	v_bfe_u32 v12, v12, 2, 2
	v_bitop3_b32 v14, v102, v100, v12 bitop3:0x36
	v_lshl_add_u64 v[12:13], v[10:11], 0, v[58:59]
	v_lshlrev_b64 v[12:13], 9, v[12:13]
	v_lshlrev_b32_e32 v16, 8, v16
	v_lshl_add_u64 v[12:13], s[4:5], 0, v[12:13]
	v_lshlrev_b32_e32 v14, 4, v14
	v_readfirstlane_b32 s12, v16
	v_add_u32_e32 v17, 0xc000, v16
	v_lshl_add_u64 v[12:13], v[12:13], 0, v[14:15]
	s_mov_b32 m0, s12
	v_readfirstlane_b32 s12, v17
	v_or_b32_e32 v58, 1, v58
	global_load_lds_dwordx4 v[12:13], off
	v_lshl_add_u64 v[12:13], v[12:13], 0, s[6:7]
	s_mov_b32 m0, s12
	v_lshl_add_u64 v[10:11], v[10:11], 0, v[58:59]
	global_load_lds_dwordx4 v[12:13], off
	v_lshlrev_b64 v[10:11], 9, v[10:11]
	v_add_u32_e32 v12, 0x6000, v16
	v_lshl_add_u64 v[10:11], s[4:5], 0, v[10:11]
	v_readfirstlane_b32 s4, v12
	v_add_u32_e32 v12, 0x12000, v16
	v_lshl_add_u64 v[10:11], v[10:11], 0, v[14:15]
	s_mov_b32 m0, s4
	v_readfirstlane_b32 s4, v12
	global_load_lds_dwordx4 v[10:11], off
	v_lshl_add_u64 v[10:11], v[10:11], 0, s[6:7]
	s_mov_b32 m0, s4
	s_nop 0
	global_load_lds_dwordx4 v[10:11], off
	s_waitcnt lgkmcnt(0)
	s_barrier
	v_lshlrev_b32_e32 v10, 2, v0
	v_and_b32_e32 v94, 12, v10
	v_or_b32_e32 v120, v94, v61
	v_bitop3_b32 v10, v124, v94, v61 bitop3:0x1e
	v_lshl_or_b32 v14, v10, 4, v18
	v_bitop3_b32 v10, v124, v120, 1 bitop3:0x36
	v_lshl_or_b32 v19, v10, 4, v18
	ds_read_b128 v[10:13], v14
	ds_read_b128 v[62:65], v14 offset:8192
	ds_read_b128 v[14:17], v19
	ds_read_b128 v[66:69], v19 offset:8192
	v_bitop3_b32 v19, v124, v120, 4 bitop3:0x36
	v_lshl_or_b32 v19, v19, 4, v18
	v_bitop3_b32 v20, v124, v120, 5 bitop3:0x36
	v_lshl_or_b32 v20, v20, 4, v18
	ds_read_b128 v[70:73], v19
	ds_read_b128 v[78:81], v19 offset:8192
	ds_read_b128 v[74:77], v20
	ds_read_b128 v[82:85], v20 offset:8192
	v_bitop3_b32 v19, v124, v120, 8 bitop3:0x36
	v_lshl_or_b32 v19, v19, 4, v18
	v_bitop3_b32 v20, v124, v120, 9 bitop3:0x36
	v_lshl_or_b32 v20, v20, 4, v18
	ds_read_b128 v[86:89], v19
	ds_read_b128 v[104:107], v19 offset:8192
	ds_read_b128 v[90:93], v20
	ds_read_b128 v[108:111], v20 offset:8192
	v_bitop3_b32 v19, v124, v120, 12 bitop3:0x36
	v_lshl_or_b32 v19, v19, 4, v18
	v_bitop3_b32 v20, v124, v120, 13 bitop3:0x36
	v_lshl_or_b32 v18, v20, 4, v18
	ds_read_b128 v[126:129], v19
	ds_read_b128 v[134:137], v19 offset:8192
	ds_read_b128 v[130:133], v18
	ds_read_b128 v[138:141], v18 offset:8192
	v_mov_b32_e32 v103, 0x7f
	v_lshlrev_b32_e32 v58, 7, v99
	v_or_b32_e32 v122, 0x18000, v117
	s_waitcnt vmcnt(18) lgkmcnt(0)
	v_mfma_scale_f32_32x32x64_f8f6f4 v[18:33], v[2:9], v[10:17], 0, v103, v103 op_sel_hi:[0,0,0]
	v_lshlrev_b32_e32 v125, 3, v119
	v_or_b32_e32 v123, 0x1a000, v117
	v_mfma_scale_f32_32x32x64_f8f6f4 v[2:17], v[2:9], v[62:69], 0, v103, v103 op_sel_hi:[0,0,0]
	v_and_b32_e32 v62, 12, v95
	s_waitcnt vmcnt(16)
	v_mfma_scale_f32_32x32x64_f8f6f4 v[18:33], v[50:57], v[70:77], v[18:33], v103, v103 op_sel_hi:[0,0,0]
	v_mfma_scale_f32_32x32x64_f8f6f4 v[2:17], v[50:57], v[78:85], v[2:17], v103, v103 op_sel_hi:[0,0,0]
	s_brev_b32 s10, 60
	v_lshlrev_b32_e32 v58, 6, v0
	v_and_b32_e32 v58, 0x4000, v58
	v_or3_b32 v63, v122, v58, v125
	v_or3_b32 v58, v123, v58, v125
	s_waitcnt vmcnt(14)
	v_mfma_scale_f32_32x32x64_f8f6f4 v[18:33], v[42:49], v[86:93], v[18:33], v103, v103 op_sel_hi:[0,0,0]
	v_mfma_scale_f32_32x32x64_f8f6f4 v[2:17], v[42:49], v[104:111], v[2:17], v103, v103 op_sel_hi:[0,0,0]
	s_nop 0
	s_waitcnt vmcnt(12)
	v_mfma_scale_f32_32x32x64_f8f6f4 v[2:17], v[34:41], v[134:141], v[2:17], v103, v103 op_sel_hi:[0,0,0]
	v_mfma_scale_f32_32x32x64_f8f6f4 v[18:33], v[34:41], v[126:133], v[18:33], v103, v103 op_sel_hi:[0,0,0]
	s_waitcnt vmcnt(8)
	s_nop 15
	s_nop 1
	v_fma_f32 v2, v2, s10, v184
	v_fma_f32 v3, v3, s10, v185
	v_fma_f32 v4, v4, s10, v186
	v_fma_f32 v5, v5, s10, v187
	v_cvt_pk_f16_f32 v2, v2, v3
	v_cvt_pk_f16_f32 v3, v4, v5
	v_bitop3_b32 v4, v95, v120, 12 bitop3:0x6c
	v_pk_fma_f32 v[18:19], v[18:19], s[10:11], v[184:185] op_sel_hi:[1,0,1]
	v_pk_fma_f32 v[20:21], v[20:21], s[10:11], v[186:187] op_sel_hi:[1,0,1]
	v_lshlrev_b32_e32 v4, 4, v4
	v_cvt_pk_f16_f32 v18, v18, v19
	v_cvt_pk_f16_f32 v19, v20, v21
	v_or_b32_e32 v5, v63, v4
	v_or_b32_e32 v4, v58, v4
	ds_write_b64 v5, v[18:19]
	ds_write_b64 v4, v[2:3]
	v_pk_fma_f32 v[2:3], v[22:23], s[10:11], v[188:189] op_sel_hi:[1,0,1]
	v_pk_fma_f32 v[4:5], v[6:7], s[10:11], v[188:189] op_sel_hi:[1,0,1]
	v_pk_fma_f32 v[6:7], v[24:25], s[10:11], v[190:191] op_sel_hi:[1,0,1]
	v_cvt_pk_f16_f32 v2, v2, v3
	v_cvt_pk_f16_f32 v3, v6, v7
	v_pk_fma_f32 v[6:7], v[8:9], s[10:11], v[190:191] op_sel_hi:[1,0,1]
	v_cvt_pk_f16_f32 v4, v4, v5
	v_cvt_pk_f16_f32 v5, v6, v7
	v_bitop3_b32 v6, v62, v120, 1 bitop3:0x36
	v_lshlrev_b32_e32 v6, 4, v6
	v_or_b32_e32 v7, v63, v6
	ds_write_b64 v7, v[2:3]
	v_or_b32_e32 v2, v58, v6
	ds_write_b64 v2, v[4:5]
	v_pk_fma_f32 v[2:3], v[26:27], s[10:11], v[192:193] op_sel_hi:[1,0,1]
	v_pk_fma_f32 v[6:7], v[28:29], s[10:11], v[194:195] op_sel_hi:[1,0,1]
	v_cvt_pk_f16_f32 v2, v2, v3
	v_pk_fma_f32 v[4:5], v[10:11], s[10:11], v[192:193] op_sel_hi:[1,0,1]
	v_cvt_pk_f16_f32 v3, v6, v7
	v_pk_fma_f32 v[6:7], v[12:13], s[10:11], v[194:195] op_sel_hi:[1,0,1]
	v_cvt_pk_f16_f32 v4, v4, v5
	v_cvt_pk_f16_f32 v5, v6, v7
	v_bitop3_b32 v6, v62, v120, 2 bitop3:0x36
	v_lshlrev_b32_e32 v6, 4, v6
	v_or_b32_e32 v7, v63, v6
	ds_write_b64 v7, v[2:3]
	v_or_b32_e32 v2, v58, v6
	ds_write_b64 v2, v[4:5]
	v_pk_fma_f32 v[2:3], v[30:31], s[10:11], v[196:197] op_sel_hi:[1,0,1]
	v_pk_fma_f32 v[6:7], v[32:33], s[10:11], v[198:199] op_sel_hi:[1,0,1]
	v_cvt_pk_f16_f32 v2, v2, v3
	v_pk_fma_f32 v[4:5], v[14:15], s[10:11], v[196:197] op_sel_hi:[1,0,1]
	v_cvt_pk_f16_f32 v3, v6, v7
	v_pk_fma_f32 v[6:7], v[16:17], s[10:11], v[198:199] op_sel_hi:[1,0,1]
	v_cvt_pk_f16_f32 v4, v4, v5
	v_cvt_pk_f16_f32 v5, v6, v7
	v_bitop3_b32 v6, v62, v120, 3 bitop3:0x36
	v_lshlrev_b32_e32 v6, 4, v6
	v_or_b32_e32 v7, v63, v6
	ds_write_b64 v7, v[2:3]
	v_or_b32_e32 v2, v58, v6
	ds_write_b64 v2, v[4:5]
	s_waitcnt vmcnt(0) lgkmcnt(0)
	s_barrier
	v_and_b32_e32 v236, 1, v101
	v_lshrrev_b32_e32 v237, 1, v101
	v_xor_b32_e32 v237, v237, v236
	v_lshl_or_b32 v236, v236, 1, v237
	v_lshrrev_b32_e32 v27, 8, v0
	v_lshrrev_b32_e32 v3, 3, v0
	v_and_b32_e32 v3, 16, v3
	v_mul_u32_u24_e32 v28, 0x60, v27
	v_lshlrev_b32_e32 v26, 5, v27
	v_or_b32_e32 v146, v3, v100
	v_or_b32_e32 v147, v28, v100
	v_or_b32_e32 v4, v146, v26
	v_lshlrev_b32_e32 v209, 2, v4
	v_add_u32_e32 v209, 0x27800, v209
	v_lshlrev_b32_e32 v4, 8, v4
	v_or_b32_e32 v5, 0x18000, v4
	v_bitop3_b32 v11, v236, v120, 12 bitop3:0x36
	v_or_b32_e32 v95, 0x1c000, v4
	v_lshlrev_b32_e32 v29, 3, v101
	v_bitop3_b32 v6, v236, v94, v61 bitop3:0x1e
	v_bitop3_b32 v8, v236, v120, 4 bitop3:0x36
	v_bitop3_b32 v10, v236, v120, 8 bitop3:0x36
	v_lshlrev_b32_e32 v94, 4, v11
	v_lshlrev_b32_e32 v6, 4, v6
	v_lshlrev_b32_e32 v8, 4, v8
	v_lshlrev_b32_e32 v58, 4, v10
	v_or_b32_e32 v7, v5, v6
	v_or_b32_e32 v9, v5, v8
	v_or_b32_e32 v10, v5, v58
	v_or_b32_e32 v5, v5, v94
	v_or_b32_e32 v6, v95, v6
	v_or_b32_e32 v60, v95, v8
	ds_read_b128 v[22:25], v7
	ds_read_b128 v[18:21], v9
	ds_read_b128 v[14:17], v10
	ds_read_b128 v[10:13], v5
	ds_read_b128 v[6:9], v6
	ds_read_b128 v[2:5], v60
	v_bfe_u32 v103, v0, 6, 1
	s_movk_i32 s5, 0x2000
	v_mad_u32_u24 v44, v103, 48, v147
	v_lshlrev_b32_e32 v60, 8, v44
	v_lshlrev_b32_e32 v44, 2, v44
	v_or_b32_e32 v35, v95, v58
	v_lshlrev_b32_e32 v58, 14, v99
	v_and_b32_e32 v44, 12, v44
	v_or_b32_e32 v56, v44, v61
	v_bitop3_b32 v44, v236, v44, v61 bitop3:0x1e
	v_lshl_add_u64 v[32:33], s[8:9], 0, v[58:59]
	v_lshlrev_b32_e32 v58, 4, v98
	v_or_b32_e32 v36, v95, v94
	v_lshl_add_u64 v[88:89], v[32:33], 0, v[58:59]
	v_lshl_or_b32 v57, v44, 4, v60
	ds_read_b128 v[40:43], v35
	ds_read_b128 v[106:109], v36
	global_load_dwordx4 v[36:39], v[88:89], off
	global_load_dwordx4 v[32:35], v[88:89], off offset:1024
	ds_read_b128 v[44:47], v57
	v_bitop3_b32 v48, v236, v56, 4 bitop3:0x36
	v_lshl_or_b32 v62, v48, 4, v60
	ds_read_b128 v[48:51], v62
	v_bitop3_b32 v52, v236, v56, 8 bitop3:0x36
	v_lshl_or_b32 v63, v52, 4, v60
	ds_read_b128 v[52:55], v63
	s_waitcnt lgkmcnt(0)
	v_mfma_f32_16x16x32_f16 v[44:47], v[44:47], v[22:25], 0
	v_bitop3_b32 v64, v236, v56, 12 bitop3:0x36
	ds_read_b128 v[56:59], v57 offset:49152
	v_lshl_or_b32 v60, v64, 4, v60
	v_mfma_f32_16x16x32_f16 v[44:47], v[48:51], v[18:21], v[44:47]
	ds_read_b128 v[68:71], v60
	ds_read_b128 v[72:75], v62 offset:49152
	v_mad_u32_u24 v104, v103, 3, 1
	v_lshlrev_b32_e32 v132, 4, v104
	v_mfma_f32_16x16x32_f16 v[44:47], v[52:55], v[14:17], v[44:47]
	v_add_u32_e32 v52, v132, v147
	global_load_dwordx4 v[64:67], v[88:89], off offset:2048
	global_load_dwordx4 v[48:51], v[88:89], off offset:3072
	ds_read_b128 v[76:79], v63 offset:49152
	ds_read_b128 v[80:83], v60 offset:49152
	s_waitcnt lgkmcnt(3)
	v_mfma_f32_16x16x32_f16 v[44:47], v[68:71], v[10:13], v[44:47]
	v_lshlrev_b32_e32 v60, 8, v52
	v_lshlrev_b32_e32 v52, 2, v52
	v_and_b32_e32 v52, 12, v52
	v_mfma_f32_16x16x32_f16 v[44:47], v[56:59], v[6:9], v[44:47]
	v_or_b32_e32 v62, v52, v61
	v_bitop3_b32 v52, v236, v52, v61 bitop3:0x1e
	v_lshl_or_b32 v63, v52, 4, v60
	s_waitcnt lgkmcnt(2)
	v_mfma_f32_16x16x32_f16 v[44:47], v[72:75], v[2:5], v[44:47]
	ds_read_b128 v[52:55], v63
	v_bitop3_b32 v56, v236, v62, 4 bitop3:0x36
	v_lshl_or_b32 v84, v56, 4, v60
	s_waitcnt lgkmcnt(2)
	v_mfma_f32_16x16x32_f16 v[44:47], v[76:79], v[40:43], v[44:47]
	ds_read_b128 v[56:59], v84
	v_bitop3_b32 v68, v236, v62, 8 bitop3:0x36
	v_lshl_or_b32 v85, v68, 4, v60
	s_waitcnt lgkmcnt(2)
	v_mfma_f32_16x16x32_f16 v[110:113], v[80:83], v[106:109], v[44:47]
	ds_read_b128 v[68:71], v63 offset:49152
	v_bitop3_b32 v62, v236, v62, 12 bitop3:0x36
	v_lshl_or_b32 v60, v62, 4, v60
	ds_read_b128 v[44:47], v85
	s_waitcnt lgkmcnt(3)
	v_mfma_f32_16x16x32_f16 v[52:55], v[52:55], v[22:25], 0
	ds_read_b128 v[72:75], v60
	ds_read_b128 v[76:79], v84 offset:49152
	v_mad_u32_u24 v105, v103, 3, 2
	v_lshlrev_b32_e32 v133, 4, v105
	s_waitcnt lgkmcnt(4)
	v_mfma_f32_16x16x32_f16 v[52:55], v[56:59], v[18:21], v[52:55]
	ds_read_b128 v[56:59], v85 offset:49152
	v_add_co_u32_e32 v114, vcc, s15, v88
	s_waitcnt lgkmcnt(3)
	v_mfma_f32_16x16x32_f16 v[44:47], v[44:47], v[14:17], v[52:55]
	v_addc_co_u32_e32 v115, vcc, 0, v89, vcc
	s_waitcnt lgkmcnt(2)
	v_mfma_f32_16x16x32_f16 v[44:47], v[72:75], v[10:13], v[44:47]
	ds_read_b128 v[52:55], v60 offset:49152
	v_add_u32_e32 v60, v133, v147
	v_lshlrev_b32_e32 v72, 8, v60
	v_lshlrev_b32_e32 v60, 2, v60
	v_mfma_f32_16x16x32_f16 v[44:47], v[68:71], v[6:9], v[44:47]
	v_and_b32_e32 v60, 12, v60
	v_or_b32_e32 v68, v60, v61
	v_bitop3_b32 v60, v236, v60, v61 bitop3:0x1e
	v_lshl_or_b32 v69, v60, 4, v72
	s_waitcnt lgkmcnt(2)
	v_mfma_f32_16x16x32_f16 v[44:47], v[76:79], v[2:5], v[44:47]
	ds_read_b128 v[60:63], v69
	v_bitop3_b32 v70, v236, v68, 4 bitop3:0x36
	v_lshl_or_b32 v70, v70, 4, v72
	s_waitcnt lgkmcnt(2)
	v_mfma_f32_16x16x32_f16 v[44:47], v[56:59], v[40:43], v[44:47]
	ds_read_b128 v[56:59], v70
	v_bitop3_b32 v71, v236, v68, 8 bitop3:0x36
	v_lshl_or_b32 v71, v71, 4, v72
	s_waitcnt lgkmcnt(1)
	v_mfma_f32_16x16x32_f16 v[22:25], v[60:63], v[22:25], 0
	v_bitop3_b32 v60, v236, v68, 12 bitop3:0x36
	v_lshl_or_b32 v68, v60, 4, v72
	ds_read_b32 v210, v209
	v_mfma_f32_16x16x32_f16 v[126:129], v[52:55], v[106:109], v[44:47]
	s_nop 2
	ds_read_b128 v[44:47], v71
	ds_read_b128 v[52:55], v69 offset:49152
	ds_read_b128 v[60:63], v70 offset:49152
	s_waitcnt lgkmcnt(4)
	v_mfma_f32_16x16x32_f16 v[18:21], v[56:59], v[18:21], v[22:25]
	ds_read_b128 v[56:59], v71 offset:49152
	s_nop 1
	ds_read_b128 v[22:25], v68
	s_waitcnt lgkmcnt(4)
	v_mfma_f32_16x16x32_f16 v[14:17], v[44:47], v[14:17], v[18:21]
	v_add_co_u32_e32 v44, vcc, s5, v88
	s_movk_i32 s5, 0x3000
	s_nop 0
	ds_read_b128 v[18:21], v68 offset:49152
	s_waitcnt lgkmcnt(1)
	v_mfma_f32_16x16x32_f16 v[10:13], v[22:25], v[10:13], v[14:17]
	v_addc_co_u32_e32 v45, vcc, 0, v89, vcc
	global_load_dwordx4 v[84:87], v[114:115], off offset:1024
	global_load_dwordx4 v[80:83], v[114:115], off offset:2048
	global_load_dwordx4 v[92:95], v[44:45], off offset:-4096
	global_load_dwordx4 v[76:79], v[44:45], off
	v_mfma_f32_16x16x32_f16 v[6:9], v[52:55], v[6:9], v[10:13]
	global_load_dwordx4 v[72:75], v[44:45], off offset:1024
	global_load_dwordx4 v[68:71], v[44:45], off offset:2048
	global_load_dwordx4 v[52:55], v[44:45], off offset:3072
	v_mov_b32_e32 v13, 0xff61b1e6
	v_mfma_f32_16x16x32_f16 v[2:5], v[60:63], v[2:5], v[6:9]
	s_nop 2
	v_add_co_u32_e32 v6, vcc, s5, v88
	v_mfma_f32_16x16x32_f16 v[2:5], v[56:59], v[40:43], v[2:5]
	s_nop 0
	v_addc_co_u32_e32 v7, vcc, 0, v89, vcc
	global_load_dwordx4 v[88:91], v[114:115], off offset:3072
	global_load_dwordx4 v[60:63], v[6:7], off
	global_load_dwordx4 v[56:59], v[6:7], off offset:1024
	global_load_dwordx4 v[44:47], v[6:7], off offset:2048
	global_load_dwordx4 v[40:43], v[6:7], off offset:3072
	s_waitcnt lgkmcnt(0)
	v_mfma_f32_16x16x32_f16 v[16:19], v[18:21], v[106:109], v[2:5]
	s_mov_b32 s5, 0xff61b1e6
	s_nop 0
	v_or_b32_e32 v3, s14, v146
	v_mov_b32_e32 v4, 0x7df
	v_med3_u32 v3, v3, 32, v4
	v_or_b32_e32 v4, v97, v102
	v_sub_u32_e32 v3, v4, v3
	v_add_f32_e32 v2, s32, v210
	v_add_u32_e32 v3, 32, v3
	v_mad_u32_u24 v4, v103, 48, v3
	s_movk_i32 s4, 0x41
	v_add_f32_e32 v5, v2, v110
	v_mul_f32_e32 v5, 0x3db8aa3b, v5
	v_cmp_gt_u32_e32 vcc, s4, v4
	v_add_u32_e32 v6, 1, v4
	v_add_f32_e32 v7, v2, v111
	v_cndmask_b32_e32 v5, v13, v5, vcc
	v_mul_f32_e32 v7, 0x3db8aa3b, v7
	v_cmp_gt_u32_e32 vcc, s4, v6
	v_add_u32_e32 v8, 2, v4
	v_add_f32_e32 v9, v2, v112
	v_cndmask_b32_e32 v6, v13, v7, vcc
	v_mul_f32_e32 v9, 0x3db8aa3b, v9
	v_cmp_gt_u32_e32 vcc, s4, v8
	v_add_u32_e32 v4, 3, v4
	v_max3_f32 v7, v5, s5, v6
	v_cndmask_b32_e32 v8, v13, v9, vcc
	v_add_f32_e32 v9, v2, v113
	v_mul_f32_e32 v9, 0x3db8aa3b, v9
	v_cmp_gt_u32_e32 vcc, s4, v4
	v_add_u32_e32 v11, v3, v132
	v_add_f32_e32 v12, v2, v127
	v_cndmask_b32_e32 v10, v13, v9, vcc
	v_max3_f32 v4, v7, v8, v10
	v_add_f32_e32 v7, v2, v126
	v_mul_f32_e32 v7, 0x3db8aa3b, v7
	v_cmp_gt_u32_e32 vcc, s4, v11
	v_add_u32_e32 v9, 1, v11
	v_mul_f32_e32 v12, 0x3db8aa3b, v12
	v_cndmask_b32_e32 v7, v13, v7, vcc
	v_cmp_gt_u32_e32 vcc, s4, v9
	v_add_f32_e32 v14, v2, v128
	v_mul_f32_e32 v14, 0x3db8aa3b, v14
	v_cndmask_b32_e32 v9, v13, v12, vcc
	v_add_u32_e32 v12, 2, v11
	v_cmp_gt_u32_e32 vcc, s4, v12
	v_add_u32_e32 v11, 3, v11
	v_add_u32_e32 v3, v3, v133
	v_cndmask_b32_e32 v12, v13, v14, vcc
	v_add_f32_e32 v14, v2, v129
	v_mul_f32_e32 v14, 0x3db8aa3b, v14
	v_cmp_gt_u32_e32 vcc, s4, v11
	v_add_f32_e32 v11, v2, v16
	v_mul_f32_e32 v11, 0x3db8aa3b, v11
	v_cndmask_b32_e32 v15, v13, v14, vcc
	v_cmp_gt_u32_e32 vcc, s4, v3
	v_add_u32_e32 v14, 1, v3
	v_add_f32_e32 v16, v2, v17
	v_cndmask_b32_e32 v11, v13, v11, vcc
	v_mul_f32_e32 v16, 0x3db8aa3b, v16
	v_cmp_gt_u32_e32 vcc, s4, v14
	v_add_f32_e32 v17, v2, v18
	v_max3_f32 v4, v4, v7, v9
	v_cndmask_b32_e32 v14, v13, v16, vcc
	v_add_u32_e32 v16, 2, v3
	v_mul_f32_e32 v17, 0x3db8aa3b, v17
	v_cmp_gt_u32_e32 vcc, s4, v16
	v_add_u32_e32 v3, 3, v3
	v_add_f32_e32 v2, v2, v19
	v_max3_f32 v4, v4, v12, v15
	v_cndmask_b32_e32 v16, v13, v17, vcc
	v_mul_f32_e32 v2, 0x3db8aa3b, v2
	v_cmp_gt_u32_e32 vcc, s4, v3
	v_max3_f32 v4, v4, v11, v14
	v_lshlrev_b32_e32 v126, 5, v99
	v_cndmask_b32_e32 v17, v13, v2, vcc
	v_max3_f32 v2, v4, v16, v17
	v_mov_b32_e32 v3, v2
	v_lshlrev_b32_e32 v127, 2, v119
	v_lshrrev_b32_e32 v4, 7, v0
	v_cmp_gt_u32_e32 vcc, 16, v98
	v_permlane16_swap_b32_e32 v3, v2
	v_max_f32_e32 v2, v2, v3
	v_mov_b32_e32 v3, v2
	s_nop 1
	v_permlane32_swap_b32_e32 v3, v2
	v_max_f32_e32 v13, v2, v3
	v_and_b32_e32 v2, 0x180, v0
	v_or_b32_e32 v2, 0x23400, v2
	v_lshlrev_b32_e32 v3, 2, v100
	s_and_saveexec_b64 s[4:5], vcc
	v_lshlrev_b32_e32 v18, 6, v103
	v_add3_u32 v18, v2, v18, v3
	ds_write_b32 v18, v13
	s_or_b64 exec, exec, s[4:5]
	v_lshlrev_b32_e32 v18, 4, v103
	v_bitop3_b32 v19, v18, 16, v100 bitop3:0x36
	v_lshl_add_u32 v2, v19, 2, v2
	s_waitcnt lgkmcnt(0)
	s_barrier
	ds_read_b32 v19, v2
	v_max_f32_e32 v13, v13, v13
	v_mul_u32_u24_e32 v20, 0xd00, v4
	v_or_b32_e32 v2, 1, v124
	s_waitcnt lgkmcnt(0)
	v_max_f32_e32 v19, v19, v19
	v_max_f32_e32 v19, v13, v19
	v_sub_f32_e32 v5, v5, v19
	v_exp_f32_e32 v5, v5
	v_sub_f32_e32 v6, v6, v19
	v_exp_f32_e32 v6, v6
	v_sub_f32_e32 v8, v8, v19
	v_mul_u32_u24_e32 v13, 0xd0, v100
	v_exp_f32_e32 v8, v8
	v_sub_f32_e32 v10, v10, v19
	v_add3_u32 v20, v13, v20, v29
	v_exp_f32_e32 v10, v10
	v_or_b32_e32 v22, 0x20000, v20
	v_add_f32_e32 v20, 0, v5
	v_add_f32_e32 v20, v20, v6
	v_add_f32_e32 v20, v20, v8
	v_add_f32_e32 v23, v20, v10
	v_cvt_pk_f16_f32 v21, v8, v10
	v_cvt_pk_f16_f32 v20, v5, v6
	v_mad_u32_u24 v5, v103, s16, v22
	ds_write_b64 v5, v[20:21]
	v_sub_f32_e32 v5, v7, v19
	v_exp_f32_e32 v5, v5
	v_sub_f32_e32 v6, v9, v19
	v_exp_f32_e32 v6, v6
	v_sub_f32_e32 v7, v12, v19
	v_exp_f32_e32 v7, v7
	v_sub_f32_e32 v8, v15, v19
	v_exp_f32_e32 v8, v8
	v_sub_f32_e32 v10, v11, v19
	v_add_f32_e32 v9, v23, v5
	v_exp_f32_e32 v10, v10
	v_sub_f32_e32 v11, v14, v19
	v_add_f32_e32 v9, v9, v6
	v_exp_f32_e32 v11, v11
	v_sub_f32_e32 v12, v16, v19
	v_add_f32_e32 v9, v9, v7
	v_exp_f32_e32 v12, v12
	v_sub_f32_e32 v14, v17, v19
	v_add_f32_e32 v9, v9, v8
	v_exp_f32_e32 v14, v14
	v_add_f32_e32 v9, v9, v10
	v_add_f32_e32 v9, v9, v11
	v_add_f32_e32 v9, v9, v12
	v_add_f32_e32 v9, v9, v14
	v_mov_b32_e32 v15, v9
	v_cvt_pk_f16_f32 v7, v7, v8
	v_cvt_pk_f16_f32 v6, v5, v6
	v_lshl_add_u32 v5, v104, 5, v22
	ds_write_b64 v5, v[6:7]
	v_permlane16_swap_b32_e32 v15, v9
	v_add_f32_e32 v5, v9, v15
	v_mov_b32_e32 v6, v5
	s_movk_i32 s7, 0xd00
	s_mov_b32 s6, 0x20000
	v_cvt_pk_f16_f32 v9, v12, v14
	v_cvt_pk_f16_f32 v8, v10, v11
	v_lshl_add_u32 v7, v105, 5, v22
	ds_write_b64 v7, v[8:9]
	v_permlane32_swap_b32_e32 v6, v5
	s_and_saveexec_b64 s[4:5], vcc
	s_cbranch_execz .LBB1_4
	v_lshlrev_b32_e32 v4, 5, v4
	v_or_b32_e32 v7, v18, v100
	v_lshlrev_b32_e32 v4, 2, v4
	v_lshlrev_b32_e32 v7, 2, v7
	s_mov_b32 s8, 0x23600
	v_add3_u32 v4, v7, v4, s8
	v_add_f32_e32 v5, v5, v6
	ds_write_b32 v4, v5

	.amdhsa_kernel _Z7na_mainPKDF16_PKhS0_PKfS4_S4_S4_Pf
		.amdhsa_group_segment_fixed_size 162048
		.amdhsa_private_segment_fixed_size 0
		.amdhsa_kernarg_size 64
		.amdhsa_user_sgpr_count 2
		.amdhsa_user_sgpr_dispatch_ptr 0
		.amdhsa_user_sgpr_queue_ptr 0
		.amdhsa_user_sgpr_kernarg_segment_ptr 1
		.amdhsa_user_sgpr_dispatch_id 0
		.amdhsa_user_sgpr_kernarg_preload_length 0
		.amdhsa_user_sgpr_kernarg_preload_offset 0
		.amdhsa_user_sgpr_private_segment_size 0
		.amdhsa_uses_dynamic_stack 0
		.amdhsa_enable_private_segment 0
		.amdhsa_system_sgpr_workgroup_id_x 1
		.amdhsa_system_sgpr_workgroup_id_y 0
		.amdhsa_system_sgpr_workgroup_id_z 0
		.amdhsa_system_sgpr_workgroup_info 0
		.amdhsa_system_vgpr_workitem_id 0
		.amdhsa_next_free_vgpr 252
		.amdhsa_next_free_sgpr 96
		.amdhsa_accum_offset 252
		.amdhsa_reserve_vcc 1
		.amdhsa_float_round_mode_32 0
		.amdhsa_float_round_mode_16_64 0
		.amdhsa_float_denorm_mode_32 3
		.amdhsa_float_denorm_mode_16_64 3
		.amdhsa_dx10_clamp 1
		.amdhsa_ieee_mode 1
		.amdhsa_fp16_overflow 0
		.amdhsa_tg_split 0
		.amdhsa_exception_fp_ieee_invalid_op 0
		.amdhsa_exception_fp_denorm_src 0
		.amdhsa_exception_fp_ieee_div_zero 0
		.amdhsa_exception_fp_ieee_overflow 0
		.amdhsa_exception_fp_ieee_underflow 0
		.amdhsa_exception_fp_ieee_inexact 0
		.amdhsa_exception_int_div_zero 0
	.end_amdhsa_kernel

amdhsa.kernels:
  - .agpr_count:     16
    .args:
      - .actual_access:  read_only
        .address_space:  global
        .offset:         0
        .size:           8
        .value_kind:     global_buffer
      - .actual_access:  read_only
        .address_space:  global
        .offset:         8
        .size:           8
        .value_kind:     global_buffer
      - .actual_access:  read_only
        .address_space:  global
        .offset:         16
        .size:           8
        .value_kind:     global_buffer
      - .actual_access:  read_only
        .address_space:  global
        .offset:         24
        .size:           8
        .value_kind:     global_buffer
      - .actual_access:  read_only
        .address_space:  global
        .offset:         32
        .size:           8
        .value_kind:     global_buffer
      - .actual_access:  read_only
        .address_space:  global
        .offset:         40
        .size:           8
        .value_kind:     global_buffer
      - .actual_access:  write_only
        .address_space:  global
        .offset:         48
        .size:           8
        .value_kind:     global_buffer
      - .actual_access:  write_only
        .address_space:  global
        .offset:         56
        .size:           8
        .value_kind:     global_buffer
      - .actual_access:  write_only
        .address_space:  global
        .offset:         64
        .size:           8
        .value_kind:     global_buffer
      - .actual_access:  write_only
        .address_space:  global
        .offset:         72
        .size:           8
        .value_kind:     global_buffer
      - .actual_access:  write_only
        .address_space:  global
        .offset:         80
        .size:           8
        .value_kind:     global_buffer
      - .actual_access:  write_only
        .address_space:  global
        .offset:         88
        .size:           8
        .value_kind:     global_buffer
    .group_segment_fixed_size: 50176
    .kernarg_segment_align: 8
    .kernarg_segment_size: 96
    .language:       OpenCL C
    .language_version:
      - 2
      - 0
    .max_flat_workgroup_size: 256
    .name:           _Z7na_prepPKfS0_S0_S0_S0_S0_PDF16_PhS1_PfS3_S3_
    .private_segment_fixed_size: 0
    .sgpr_count:     23
    .sgpr_spill_count: 0
    .symbol:         _Z7na_prepPKfS0_S0_S0_S0_S0_PDF16_PhS1_PfS3_S3_.kd
    .uniform_work_group_size: 1
    .uses_dynamic_stack: false
    .vgpr_count:     116
    .vgpr_spill_count: 0
    .wavefront_size: 64
  - .agpr_count:     0
    .args:
      - .address_space:  global
        .offset:         0
        .size:           8
        .value_kind:     global_buffer
      - .actual_access:  read_only
        .address_space:  global
        .offset:         8
        .size:           8
        .value_kind:     global_buffer
      - .actual_access:  read_only
        .address_space:  global
        .offset:         16
        .size:           8
        .value_kind:     global_buffer
      - .actual_access:  read_only
        .address_space:  global
        .offset:         24
        .size:           8
        .value_kind:     global_buffer
      - .actual_access:  read_only
        .address_space:  global
        .offset:         32
        .size:           8
        .value_kind:     global_buffer
      - .actual_access:  read_only
        .address_space:  global
        .offset:         40
        .size:           8
        .value_kind:     global_buffer
      - .actual_access:  read_only
        .address_space:  global
        .offset:         48
        .size:           8
        .value_kind:     global_buffer
      - .actual_access:  write_only
        .address_space:  global
        .offset:         56
        .size:           8
        .value_kind:     global_buffer
    .group_segment_fixed_size: 162048
    .kernarg_segment_align: 8
    .kernarg_segment_size: 64
    .language:       OpenCL C
    .language_version:
      - 2
      - 0
    .max_flat_workgroup_size: 512
    .name:           _Z7na_mainPKDF16_PKhS0_PKfS4_S4_S4_Pf
    .private_segment_fixed_size: 0
    .sgpr_count:     24
    .sgpr_spill_count: 0
    .symbol:         _Z7na_mainPKDF16_PKhS0_PKfS4_S4_S4_Pf.kd
    .uniform_work_group_size: 1
    .uses_dynamic_stack: false
    .vgpr_count:     252
    .vgpr_spill_count: 0
    .wavefront_size: 64
